# batch 3 plus non-temporal stores for the expert hidden activations (ACT) written by M1
# speedup vs baseline: 1.0861x; 1.0231x over previous
; #define LAS __attribute__((address_space(3)))
;     DI void operator()(const f32x4 (&acc)[2][2][4][2], const Unit& u, int wr, int wc, int fr, int fq) const {
;         int lrow = 64 * wr + fr; asm volatile("" : "+v"(lrow));
;         const int cj = u.pn * 128 + 32 * wc + 8 * fq; const LAS float* bb = bl + 32 * wc + 8 * fq;
;         const f32x4 bg0 = *(const LAS f32x4*)(bb), bg1 = *(const LAS f32x4*)(bb + 4), bu0 = *(const LAS f32x4*)(bb + 128), bu1 = *(const LAS f32x4*)(bb + 132);
;         unsigned char* abase = act + (size_t)u.pm * 256 * DFF;
;         constexpr float dq = 1.0f / (W8_SCALE * H8_SCALE * PROBE_KREP);
; #pragma unroll
;         for (int ai = 0; ai < 2; ++ai) { if (u.half == 2 - ai) continue;
;             u32x2 wprev = {0u, 0u}; const bool oddq = (fq & 1) != 0;
; #pragma unroll
;             for (int m = 0; m < 4; ++m) {
;             f32x4 g0 = acc[ai][0][m][0] * dq + bg0, g1 = acc[ai][0][m][1] * dq + bg1, u0 = acc[ai][1][m][0] * dq + bu0, u1 = acc[ai][1][m][1] * dq + bu1;
;             unsigned wv[2];
; #pragma unroll
;             for (int hv = 0; hv < 2; ++hv) { const f32x4 gq = hv ? g1 : g0, uq = hv ? u1 : u0; int r = 0;
; #pragma unroll
;                 for (int q = 0; q < 4; q += 2) {
;                     f32x2 g = {fminf(gq[q], 7.0f), fminf(gq[q + 1], 7.0f)};
;                     const f32x2 up = {fminf(fmaxf(uq[q], -7.0f), 7.0f), fminf(fmaxf(uq[q + 1], -7.0f), 7.0f)};
;                     f32x2 t = __builtin_elementwise_fma(up, (f32x2){ACT8_SCALE, ACT8_SCALE}, (f32x2){ACT8_SCALE, ACT8_SCALE}) * g;
;                     const f32x2 a = g * (f32x2){-1.702f * 1.4426950408889634f, -1.702f * 1.4426950408889634f};
;                     f32x2 e = {__builtin_amdgcn_exp2f(a[0]), __builtin_amdgcn_exp2f(a[1])}; e = e + (f32x2){1.0f, 1.0f};
;                     const f32x2 rc = {__builtin_amdgcn_rcpf(e[0]), __builtin_amdgcn_rcpf(e[1])};
;                     t = t * rc;
;                     r = q ? __builtin_amdgcn_cvt_pk_fp8_f32(t[0], t[1], r, true) : __builtin_amdgcn_cvt_pk_fp8_f32(t[0], t[1], r, false); }
.LBB0_1232:
	s_mov_b32 s0, -1
	s_mov_b32 s1, s56
	s_ashr_i32 s25, s24, 31
	v_mbcnt_lo_u32_b32 v0, s0, 0
	v_mbcnt_hi_u32_b32 v0, s0, v0
	s_lshl_b32 s0, s1, 4
	s_andn2_b32 s0, s0, 63
	s_nop 0
	v_and_or_b32 v23, v0, 15, s0
	s_lshl_b32 s0, s1, 5
	s_and_b32 s3, s0, 0x60
	s_lshl_b32 s0, s3, 2
	v_ashrrev_i32_e32 v18, 4, v0
	s_add_i32 s0, s0, 0
	v_lshl_add_u32 v0, v18, 5, s0
	v_add_u32_e32 v0, 0x21000, v0
	ds_read_b128 v[14:17], v0
	ds_read_b128 v[10:13], v0 offset:16
	ds_read_b128 v[6:9], v0 offset:512
	ds_read_b128 v[2:5], v0 offset:528
	s_lshl_b64 s[0:1], s[24:25], 18
	s_add_u32 s6, s97, s0
	s_addc_u32 s7, s62, s1
	v_and_b32_e32 v22, 1, v18
	s_or_b32 s0, s3, s2
	v_lshl_add_u32 v0, v18, 3, s0
	v_lshlrev_b32_e32 v18, 3, v22
	v_sub_u32_e32 v0, v0, v18
	s_and_b64 vcc, exec, s[28:29]
	v_lshlrev_b32_e32 v24, 14, v22
	v_lshlrev_b32_e32 v25, 10, v23
	s_cbranch_vccz .LBB0_1234
	s_waitcnt lgkmcnt(0)
	v_pk_fma_f32 v[32:33], v[182:183], s[52:53], v[6:7] op_sel_hi:[1,0,1]
	v_pk_fma_f32 v[18:19], v[190:191], s[52:53], v[14:15] op_sel_hi:[1,0,1]
	v_med3_f32 v32, v32, s93, v251
	v_med3_f32 v33, v33, s93, v251
	s_mov_b32 s0, 0x41000000
	v_min_f32_e32 v18, 0x40e00000, v18
	v_min_f32_e32 v19, 0x40e00000, v19
	v_pk_fma_f32 v[32:33], v[32:33], s[0:1], s[0:1] op_sel_hi:[1,0,0]
	s_mov_b32 s2, 0xc01d265f
	v_pk_mul_f32 v[32:33], v[18:19], v[32:33]
	v_pk_mul_f32 v[18:19], v[18:19], s[2:3] op_sel_hi:[1,0]
	v_pk_fma_f32 v[30:31], v[184:185], s[52:53], v[8:9] op_sel_hi:[1,0,1]
	v_exp_f32_e32 v18, v18
	v_exp_f32_e32 v19, v19
	v_pk_fma_f32 v[20:21], v[192:193], s[52:53], v[16:17] op_sel_hi:[1,0,1]
	v_med3_f32 v30, v30, s93, v251
	v_med3_f32 v31, v31, s93, v251
	v_min_f32_e32 v20, 0x40e00000, v20
	v_min_f32_e32 v21, 0x40e00000, v21
	v_pk_fma_f32 v[30:31], v[30:31], s[0:1], s[0:1] op_sel_hi:[1,0,0]
	v_pk_add_f32 v[18:19], v[18:19], 1.0 op_sel_hi:[1,0]
	v_pk_mul_f32 v[30:31], v[20:21], v[30:31]
	v_pk_mul_f32 v[20:21], v[20:21], s[2:3] op_sel_hi:[1,0]
	v_rcp_f32_e32 v18, v18
	v_exp_f32_e32 v20, v20
	v_exp_f32_e32 v21, v21
	v_rcp_f32_e32 v19, v19
	v_pk_fma_f32 v[28:29], v[186:187], s[52:53], v[10:11] op_sel_hi:[1,0,1]
	v_pk_fma_f32 v[36:37], v[178:179], s[52:53], v[2:3] op_sel_hi:[1,0,1]
	v_pk_add_f32 v[20:21], v[20:21], 1.0 op_sel_hi:[1,0]
	v_pk_mul_f32 v[32:33], v[32:33], v[18:19]
	v_mov_b32_e32 v18, v1
	v_rcp_f32_e32 v20, v20
	v_rcp_f32_e32 v21, v21
	v_cvt_pk_fp8_f32 v18, v32, v33
	v_pk_fma_f32 v[26:27], v[188:189], s[52:53], v[12:13] op_sel_hi:[1,0,1]
	v_pk_fma_f32 v[34:35], v[180:181], s[52:53], v[4:5] op_sel_hi:[1,0,1]
	v_pk_mul_f32 v[20:21], v[30:31], v[20:21]
	v_mov_b32_e32 v19, v1
	v_cvt_pk_fp8_f32 v18, v20, v21 op_sel:[0,0,1]
	v_min_f32_e32 v20, 0x40e00000, v28
	v_min_f32_e32 v21, 0x40e00000, v29
	v_med3_f32 v28, v36, s93, v251
	v_med3_f32 v29, v37, s93, v251
	v_pk_fma_f32 v[28:29], v[28:29], s[0:1], s[0:1] op_sel_hi:[1,0,0]
	v_pk_fma_f32 v[32:33], v[168:169], s[52:53], v[8:9] op_sel_hi:[1,0,1]
	v_pk_mul_f32 v[28:29], v[20:21], v[28:29]
	v_pk_mul_f32 v[20:21], v[20:21], s[2:3] op_sel_hi:[1,0]
	v_med3_f32 v32, v32, s93, v251
	v_exp_f32_e32 v20, v20
	v_exp_f32_e32 v21, v21
	v_med3_f32 v33, v33, s93, v251
	v_pk_fma_f32 v[32:33], v[32:33], s[0:1], s[0:1] op_sel_hi:[1,0,0]
	v_pk_fma_f32 v[30:31], v[170:171], s[52:53], v[10:11] op_sel_hi:[1,0,1]
	v_pk_add_f32 v[20:21], v[20:21], 1.0 op_sel_hi:[1,0]
	v_pk_fma_f32 v[38:39], v[162:163], s[52:53], v[2:3] op_sel_hi:[1,0,1]
	v_rcp_f32_e32 v20, v20
	v_rcp_f32_e32 v21, v21
	v_pk_fma_f32 v[36:37], v[164:165], s[52:53], v[4:5] op_sel_hi:[1,0,1]
	v_lshlrev_b32_e32 v22, 14, v22
	v_lshlrev_b32_e32 v23, 10, v23
	v_pk_mul_f32 v[20:21], v[28:29], v[20:21]
	v_pk_fma_f32 v[28:29], v[172:173], s[52:53], v[12:13] op_sel_hi:[1,0,1]
	v_cvt_pk_fp8_f32 v19, v20, v21
	v_min_f32_e32 v20, 0x40e00000, v26
	v_min_f32_e32 v21, 0x40e00000, v27
	v_med3_f32 v26, v34, s93, v251
	v_med3_f32 v27, v35, s93, v251
	v_pk_fma_f32 v[26:27], v[26:27], s[0:1], s[0:1] op_sel_hi:[1,0,0]
	v_pk_fma_f32 v[34:35], v[166:167], s[52:53], v[6:7] op_sel_hi:[1,0,1]
	v_pk_mul_f32 v[26:27], v[20:21], v[26:27]
	v_pk_mul_f32 v[20:21], v[20:21], s[2:3] op_sel_hi:[1,0]
	v_med3_f32 v34, v34, s93, v251
	v_exp_f32_e32 v20, v20
	v_exp_f32_e32 v21, v21
	v_med3_f32 v35, v35, s93, v251
	v_pk_fma_f32 v[34:35], v[34:35], s[0:1], s[0:1] op_sel_hi:[1,0,0]
	v_pk_add_f32 v[20:21], v[20:21], 1.0 op_sel_hi:[1,0]
	v_pk_fma_f32 v[40:41], v[130:131], s[52:53], v[2:3] op_sel_hi:[1,0,1]
	v_rcp_f32_e32 v20, v20
	v_rcp_f32_e32 v21, v21
	s_nop 0
	v_pk_mul_f32 v[20:21], v[26:27], v[20:21]
	s_nop 0
	v_cvt_pk_fp8_f32 v19, v20, v21 op_sel:[0,0,1]
	v_pk_fma_f32 v[20:21], v[174:175], s[52:53], v[14:15] op_sel_hi:[1,0,1]
	v_pk_fma_f32 v[26:27], v[176:177], s[52:53], v[16:17] op_sel_hi:[1,0,1]
	v_min_f32_e32 v20, 0x40e00000, v20
	v_min_f32_e32 v21, 0x40e00000, v21
	v_pk_mul_f32 v[34:35], v[20:21], v[34:35]
	v_pk_mul_f32 v[20:21], v[20:21], s[2:3] op_sel_hi:[1,0]
	v_min_f32_e32 v26, 0x40e00000, v26
	v_exp_f32_e32 v20, v20
	v_exp_f32_e32 v21, v21
	v_min_f32_e32 v27, 0x40e00000, v27
	v_pk_mul_f32 v[32:33], v[26:27], v[32:33]
	v_pk_mul_f32 v[26:27], v[26:27], s[2:3] op_sel_hi:[1,0]
	v_pk_add_f32 v[20:21], v[20:21], 1.0 op_sel_hi:[1,0]
	v_exp_f32_e32 v26, v26
	v_exp_f32_e32 v27, v27
	v_rcp_f32_e32 v20, v20
	v_rcp_f32_e32 v21, v21
	v_pk_add_f32 v[26:27], v[26:27], 1.0 op_sel_hi:[1,0]
	s_nop 0
	v_rcp_f32_e32 v26, v26
	v_pk_mul_f32 v[34:35], v[34:35], v[20:21]
	v_mov_b32_e32 v20, v1
	v_rcp_f32_e32 v27, v27
	v_cvt_pk_fp8_f32 v20, v34, v35
	v_mov_b32_e32 v21, v1
	v_pk_fma_f32 v[34:35], v[150:151], s[52:53], v[6:7] op_sel_hi:[1,0,1]
	v_pk_mul_f32 v[26:27], v[32:33], v[26:27]
	v_med3_f32 v34, v34, s93, v251
;     DI void operator()(const f32x4 (&acc)[2][2][4][2], const Unit& u, int wr, int wc, int fr, int fq) const {
;     ...
;         for (int ai = 0; ai < 2; ++ai) { if (u.half == 2 - ai) continue;
;             u32x2 wprev = {0u, 0u}; const bool oddq = (fq & 1) != 0;
; #pragma unroll
;             for (int m = 0; m < 4; ++m) {
;             f32x4 g0 = acc[ai][0][m][0] * dq + bg0, g1 = acc[ai][0][m][1] * dq + bg1, u0 = acc[ai][1][m][0] * dq + bu0, u1 = acc[ai][1][m][1] * dq + bu1;
;             unsigned wv[2];
; #pragma unroll
;             for (int hv = 0; hv < 2; ++hv) { const f32x4 gq = hv ? g1 : g0, uq = hv ? u1 : u0; int r = 0;
; #pragma unroll
;                 for (int q = 0; q < 4; q += 2) {
;                     f32x2 g = {fminf(gq[q], 7.0f), fminf(gq[q + 1], 7.0f)};
;                     const f32x2 up = {fminf(fmaxf(uq[q], -7.0f), 7.0f), fminf(fmaxf(uq[q + 1], -7.0f), 7.0f)};
;                     f32x2 t = __builtin_elementwise_fma(up, (f32x2){ACT8_SCALE, ACT8_SCALE}, (f32x2){ACT8_SCALE, ACT8_SCALE}) * g;
;                     const f32x2 a = g * (f32x2){-1.702f * 1.4426950408889634f, -1.702f * 1.4426950408889634f};
;                     f32x2 e = {__builtin_amdgcn_exp2f(a[0]), __builtin_amdgcn_exp2f(a[1])}; e = e + (f32x2){1.0f, 1.0f};
;                     const f32x2 rc = {__builtin_amdgcn_rcpf(e[0]), __builtin_amdgcn_rcpf(e[1])};
;                     t = t * rc;
;                     r = q ? __builtin_amdgcn_cvt_pk_fp8_f32(t[0], t[1], r, true) : __builtin_amdgcn_cvt_pk_fp8_f32(t[0], t[1], r, false); }
;                 wv[hv] = (unsigned)r; }
;             u32x2 w; w.x = wv[0]; w.y = wv[1];
;             if ((m & 1) == 0) wprev = w;
;             else {
;                 const auto rx = __builtin_amdgcn_permlane16_swap(wprev.x, w.x, false, false), ry = __builtin_amdgcn_permlane16_swap(wprev.y, w.y, false, false);
;                 u32x4 ww; ww.x = rx[0]; ww.y = ry[0]; ww.z = rx[1]; ww.w = ry[1];
;                 const unsigned off = (unsigned)((128 * ai + 16 * (m - 1 + (oddq ? 1 : 0)) + lrow) * DFF + cj - (oddq ? 8 : 0));
;                 *(u32x4*)(abase + off) = ww; }
;             asm volatile("" ::: "memory"); } }
	v_cvt_pk_fp8_f32 v20, v26, v27 op_sel:[0,0,1]
	v_min_f32_e32 v26, 0x40e00000, v30
	v_min_f32_e32 v27, 0x40e00000, v31
	v_med3_f32 v30, v38, s93, v251
	v_med3_f32 v31, v39, s93, v251
	v_pk_fma_f32 v[30:31], v[30:31], s[0:1], s[0:1] op_sel_hi:[1,0,0]
	v_permlane16_swap_b32_e32 v18, v20
	v_pk_mul_f32 v[30:31], v[26:27], v[30:31]
	v_pk_mul_f32 v[26:27], v[26:27], s[2:3] op_sel_hi:[1,0]
	v_med3_f32 v35, v35, s93, v251
	v_exp_f32_e32 v26, v26
	v_exp_f32_e32 v27, v27
	v_pk_fma_f32 v[34:35], v[34:35], s[0:1], s[0:1] op_sel_hi:[1,0,0]
	v_pk_fma_f32 v[32:33], v[152:153], s[52:53], v[8:9] op_sel_hi:[1,0,1]
	v_pk_fma_f32 v[38:39], v[146:147], s[52:53], v[2:3] op_sel_hi:[1,0,1]
	v_pk_add_f32 v[26:27], v[26:27], 1.0 op_sel_hi:[1,0]
	v_med3_f32 v32, v32, s93, v251
	v_rcp_f32_e32 v26, v26
	v_rcp_f32_e32 v27, v27
	v_med3_f32 v33, v33, s93, v251
	v_pk_fma_f32 v[32:33], v[32:33], s[0:1], s[0:1] op_sel_hi:[1,0,0]
	v_pk_mul_f32 v[26:27], v[30:31], v[26:27]
	s_nop 0
	v_cvt_pk_fp8_f32 v21, v26, v27
	v_min_f32_e32 v26, 0x40e00000, v28
	v_min_f32_e32 v27, 0x40e00000, v29
	v_med3_f32 v28, v36, s93, v251
	v_med3_f32 v29, v37, s93, v251
	v_pk_fma_f32 v[28:29], v[28:29], s[0:1], s[0:1] op_sel_hi:[1,0,0]
	v_pk_fma_f32 v[30:31], v[154:155], s[52:53], v[10:11] op_sel_hi:[1,0,1]
	v_pk_mul_f32 v[28:29], v[26:27], v[28:29]
	v_pk_mul_f32 v[26:27], v[26:27], s[2:3] op_sel_hi:[1,0]
	v_pk_fma_f32 v[36:37], v[148:149], s[52:53], v[4:5] op_sel_hi:[1,0,1]
	v_exp_f32_e32 v26, v26
	v_exp_f32_e32 v27, v27
	s_nop 0
	v_pk_add_f32 v[26:27], v[26:27], 1.0 op_sel_hi:[1,0]
	s_nop 0
	v_rcp_f32_e32 v26, v26
	v_rcp_f32_e32 v27, v27
	s_nop 0
	v_pk_mul_f32 v[26:27], v[28:29], v[26:27]
	s_nop 0
	v_cvt_pk_fp8_f32 v21, v26, v27 op_sel:[0,0,1]
	v_add3_u32 v26, v22, v23, v0
	v_pk_fma_f32 v[28:29], v[156:157], s[52:53], v[12:13] op_sel_hi:[1,0,1]
	v_permlane16_swap_b32_e32 v19, v21
	global_store_dwordx4 v26, v[18:21], s[6:7] nt
	v_add_u32_e32 v26, 0x8000, v26
	s_nop 0
	v_pk_fma_f32 v[18:19], v[158:159], s[52:53], v[14:15] op_sel_hi:[1,0,1]
	v_pk_fma_f32 v[20:21], v[160:161], s[52:53], v[16:17] op_sel_hi:[1,0,1]
	v_min_f32_e32 v18, 0x40e00000, v18
	v_min_f32_e32 v19, 0x40e00000, v19
	v_pk_mul_f32 v[34:35], v[18:19], v[34:35]
	v_pk_mul_f32 v[18:19], v[18:19], s[2:3] op_sel_hi:[1,0]
	v_min_f32_e32 v20, 0x40e00000, v20
	v_exp_f32_e32 v18, v18
	v_exp_f32_e32 v19, v19
	v_min_f32_e32 v21, 0x40e00000, v21
	v_pk_mul_f32 v[32:33], v[20:21], v[32:33]
	v_pk_mul_f32 v[20:21], v[20:21], s[2:3] op_sel_hi:[1,0]
	v_pk_add_f32 v[18:19], v[18:19], 1.0 op_sel_hi:[1,0]
	v_exp_f32_e32 v20, v20
	v_exp_f32_e32 v21, v21
	v_rcp_f32_e32 v18, v18
	v_rcp_f32_e32 v19, v19
	v_pk_add_f32 v[20:21], v[20:21], 1.0 op_sel_hi:[1,0]
	s_nop 0
	v_rcp_f32_e32 v20, v20
	v_pk_mul_f32 v[34:35], v[34:35], v[18:19]
	v_mov_b32_e32 v18, v1
	v_rcp_f32_e32 v21, v21
	v_cvt_pk_fp8_f32 v18, v34, v35
	v_mov_b32_e32 v19, v1
	v_pk_fma_f32 v[34:35], v[136:137], s[52:53], v[8:9] op_sel_hi:[1,0,1]
	v_pk_mul_f32 v[20:21], v[32:33], v[20:21]
	v_med3_f32 v34, v34, s93, v251
	v_cvt_pk_fp8_f32 v18, v20, v21 op_sel:[0,0,1]
	v_min_f32_e32 v20, 0x40e00000, v30
	v_min_f32_e32 v21, 0x40e00000, v31
	v_med3_f32 v30, v38, s93, v251
	v_med3_f32 v31, v39, s93, v251
	v_pk_fma_f32 v[30:31], v[30:31], s[0:1], s[0:1] op_sel_hi:[1,0,0]
	v_med3_f32 v35, v35, s93, v251
	v_pk_mul_f32 v[30:31], v[20:21], v[30:31]
	v_pk_mul_f32 v[20:21], v[20:21], s[2:3] op_sel_hi:[1,0]
	v_pk_fma_f32 v[34:35], v[34:35], s[0:1], s[0:1] op_sel_hi:[1,0,0]
	v_exp_f32_e32 v20, v20
	v_exp_f32_e32 v21, v21
	v_pk_fma_f32 v[32:33], v[138:139], s[52:53], v[10:11] op_sel_hi:[1,0,1]
	v_pk_fma_f32 v[38:39], v[132:133], s[52:53], v[4:5] op_sel_hi:[1,0,1]
	v_pk_add_f32 v[20:21], v[20:21], 1.0 op_sel_hi:[1,0]
	s_nop 0
	v_rcp_f32_e32 v20, v20
	v_rcp_f32_e32 v21, v21
	s_nop 0
	v_pk_mul_f32 v[20:21], v[30:31], v[20:21]
	s_nop 0
	v_cvt_pk_fp8_f32 v19, v20, v21
	v_min_f32_e32 v20, 0x40e00000, v28
	v_min_f32_e32 v21, 0x40e00000, v29
	v_med3_f32 v28, v36, s93, v251
	v_med3_f32 v29, v37, s93, v251
	v_pk_fma_f32 v[28:29], v[28:29], s[0:1], s[0:1] op_sel_hi:[1,0,0]
	v_pk_fma_f32 v[36:37], v[134:135], s[52:53], v[6:7] op_sel_hi:[1,0,1]
	v_pk_mul_f32 v[28:29], v[20:21], v[28:29]
	v_pk_mul_f32 v[20:21], v[20:21], s[2:3] op_sel_hi:[1,0]
	v_med3_f32 v36, v36, s93, v251
	v_exp_f32_e32 v20, v20
	v_exp_f32_e32 v21, v21
	v_med3_f32 v37, v37, s93, v251
	v_pk_fma_f32 v[36:37], v[36:37], s[0:1], s[0:1] op_sel_hi:[1,0,0]
	v_pk_fma_f32 v[30:31], v[140:141], s[52:53], v[12:13] op_sel_hi:[1,0,1]
	v_pk_add_f32 v[20:21], v[20:21], 1.0 op_sel_hi:[1,0]
	s_nop 0
	v_rcp_f32_e32 v20, v20
	v_rcp_f32_e32 v21, v21
	s_nop 0
	v_pk_mul_f32 v[20:21], v[28:29], v[20:21]
	s_nop 0
	v_cvt_pk_fp8_f32 v19, v20, v21 op_sel:[0,0,1]
	v_pk_fma_f32 v[20:21], v[142:143], s[52:53], v[14:15] op_sel_hi:[1,0,1]
	v_pk_fma_f32 v[28:29], v[144:145], s[52:53], v[16:17] op_sel_hi:[1,0,1]
	v_min_f32_e32 v20, 0x40e00000, v20
	v_min_f32_e32 v21, 0x40e00000, v21
	v_pk_mul_f32 v[36:37], v[20:21], v[36:37]
	v_pk_mul_f32 v[20:21], v[20:21], s[2:3] op_sel_hi:[1,0]
	v_min_f32_e32 v28, 0x40e00000, v28
	v_exp_f32_e32 v20, v20
	v_exp_f32_e32 v21, v21
	v_min_f32_e32 v29, 0x40e00000, v29
	v_pk_mul_f32 v[34:35], v[28:29], v[34:35]
	v_pk_mul_f32 v[28:29], v[28:29], s[2:3] op_sel_hi:[1,0]
	v_pk_add_f32 v[20:21], v[20:21], 1.0 op_sel_hi:[1,0]
	v_exp_f32_e32 v28, v28
	v_exp_f32_e32 v29, v29
	v_rcp_f32_e32 v20, v20
	v_rcp_f32_e32 v21, v21
	v_pk_add_f32 v[28:29], v[28:29], 1.0 op_sel_hi:[1,0]
	s_nop 0
	v_rcp_f32_e32 v28, v28
	v_pk_mul_f32 v[36:37], v[36:37], v[20:21]
	v_mov_b32_e32 v20, v1
	v_rcp_f32_e32 v29, v29
	v_cvt_pk_fp8_f32 v20, v36, v37
	v_mov_b32_e32 v21, v1
	v_pk_mul_f32 v[28:29], v[34:35], v[28:29]
	s_nop 0
	v_cvt_pk_fp8_f32 v20, v28, v29 op_sel:[0,0,1]
	v_min_f32_e32 v28, 0x40e00000, v32
	v_min_f32_e32 v29, 0x40e00000, v33
	v_med3_f32 v32, v40, s93, v251
	v_med3_f32 v33, v41, s93, v251
	v_pk_fma_f32 v[32:33], v[32:33], s[0:1], s[0:1] op_sel_hi:[1,0,0]
	v_permlane16_swap_b32_e32 v18, v20
	v_pk_mul_f32 v[32:33], v[28:29], v[32:33]
	v_pk_mul_f32 v[28:29], v[28:29], s[2:3] op_sel_hi:[1,0]
	s_nop 0
	v_exp_f32_e32 v28, v28
	v_exp_f32_e32 v29, v29
	s_nop 0
	v_pk_add_f32 v[28:29], v[28:29], 1.0 op_sel_hi:[1,0]
	s_nop 0
	v_rcp_f32_e32 v28, v28
	v_rcp_f32_e32 v29, v29
	s_nop 0
	v_pk_mul_f32 v[28:29], v[32:33], v[28:29]
	s_nop 0
	v_cvt_pk_fp8_f32 v21, v28, v29
	v_min_f32_e32 v28, 0x40e00000, v30
	v_min_f32_e32 v29, 0x40e00000, v31
	v_med3_f32 v30, v38, s93, v251
	v_med3_f32 v31, v39, s93, v251
	v_pk_fma_f32 v[30:31], v[30:31], s[0:1], s[0:1] op_sel_hi:[1,0,0]
	s_nop 0
	v_pk_mul_f32 v[30:31], v[28:29], v[30:31]
	v_pk_mul_f32 v[28:29], v[28:29], s[2:3] op_sel_hi:[1,0]
	s_nop 0
	v_exp_f32_e32 v28, v28
	v_exp_f32_e32 v29, v29
	s_nop 0
	v_pk_add_f32 v[28:29], v[28:29], 1.0 op_sel_hi:[1,0]
	s_nop 0
	v_rcp_f32_e32 v28, v28
	v_rcp_f32_e32 v29, v29
	s_nop 0
	v_pk_mul_f32 v[28:29], v[30:31], v[28:29]
	s_nop 0
	v_cvt_pk_fp8_f32 v21, v28, v29 op_sel:[0,0,1]
	s_nop 1
	v_permlane16_swap_b32_e32 v19, v21
	global_store_dwordx4 v26, v[18:21], s[6:7] nt
	s_cbranch_execz .LBB0_1235
;     DI void operator()(const f32x4 (&acc)[2][2][4][2], const Unit& u, int wr, int wc, int fr, int fq) const {
;     ...
; #pragma unroll
;         for (int ai = 0; ai < 2; ++ai) { if (u.half == 2 - ai) continue;
;             u32x2 wprev = {0u, 0u}; const bool oddq = (fq & 1) != 0;
; #pragma unroll
;             for (int m = 0; m < 4; ++m) {
	s_branch .LBB0_1236

;     DI void operator()(const f32x4 (&acc)[2][2][4][2], const Unit& u, int wr, int wc, int fr, int fq) const {
;     ...
;         for (int ai = 0; ai < 2; ++ai) { if (u.half == 2 - ai) continue;
;             u32x2 wprev = {0u, 0u}; const bool oddq = (fq & 1) != 0;
; #pragma unroll
;             for (int m = 0; m < 4; ++m) {
;             f32x4 g0 = acc[ai][0][m][0] * dq + bg0, g1 = acc[ai][0][m][1] * dq + bg1, u0 = acc[ai][1][m][0] * dq + bu0, u1 = acc[ai][1][m][1] * dq + bu1;
;             unsigned wv[2];
; #pragma unroll
;             for (int hv = 0; hv < 2; ++hv) { const f32x4 gq = hv ? g1 : g0, uq = hv ? u1 : u0; int r = 0;
; #pragma unroll
;                 for (int q = 0; q < 4; q += 2) {
;                     f32x2 g = {fminf(gq[q], 7.0f), fminf(gq[q + 1], 7.0f)};
;                     const f32x2 up = {fminf(fmaxf(uq[q], -7.0f), 7.0f), fminf(fmaxf(uq[q + 1], -7.0f), 7.0f)};
;                     f32x2 t = __builtin_elementwise_fma(up, (f32x2){ACT8_SCALE, ACT8_SCALE}, (f32x2){ACT8_SCALE, ACT8_SCALE}) * g;
;                     const f32x2 a = g * (f32x2){-1.702f * 1.4426950408889634f, -1.702f * 1.4426950408889634f};
;                     f32x2 e = {__builtin_amdgcn_exp2f(a[0]), __builtin_amdgcn_exp2f(a[1])}; e = e + (f32x2){1.0f, 1.0f};
;                     const f32x2 rc = {__builtin_amdgcn_rcpf(e[0]), __builtin_amdgcn_rcpf(e[1])};
;                     t = t * rc;
;                     r = q ? __builtin_amdgcn_cvt_pk_fp8_f32(t[0], t[1], r, true) : __builtin_amdgcn_cvt_pk_fp8_f32(t[0], t[1], r, false); }
;                 wv[hv] = (unsigned)r; }
.LBB0_1236:
	s_andn2_b64 vcc, exec, s[22:23]
	s_cbranch_vccnz .LBB0_1238
	s_waitcnt lgkmcnt(0)
	v_pk_fma_f32 v[30:31], v[118:119], s[52:53], v[6:7] op_sel_hi:[1,0,1]
	v_pk_fma_f32 v[18:19], v[126:127], s[52:53], v[14:15] op_sel_hi:[1,0,1]
	v_med3_f32 v30, v30, s93, v251
	v_med3_f32 v31, v31, s93, v251
	s_mov_b32 s0, 0x41000000
	v_min_f32_e32 v18, 0x40e00000, v18
	v_min_f32_e32 v19, 0x40e00000, v19
	v_pk_fma_f32 v[30:31], v[30:31], s[0:1], s[0:1] op_sel_hi:[1,0,0]
	s_mov_b32 s2, 0xc01d265f
	v_pk_mul_f32 v[30:31], v[18:19], v[30:31]
	v_pk_mul_f32 v[18:19], v[18:19], s[2:3] op_sel_hi:[1,0]
	v_pk_fma_f32 v[28:29], v[120:121], s[52:53], v[8:9] op_sel_hi:[1,0,1]
	v_exp_f32_e32 v18, v18
	v_exp_f32_e32 v19, v19
	v_pk_fma_f32 v[20:21], v[128:129], s[52:53], v[16:17] op_sel_hi:[1,0,1]
	v_med3_f32 v28, v28, s93, v251
	v_med3_f32 v29, v29, s93, v251
	v_min_f32_e32 v20, 0x40e00000, v20
	v_min_f32_e32 v21, 0x40e00000, v21
	v_pk_fma_f32 v[28:29], v[28:29], s[0:1], s[0:1] op_sel_hi:[1,0,0]
	v_pk_add_f32 v[18:19], v[18:19], 1.0 op_sel_hi:[1,0]
	v_pk_mul_f32 v[28:29], v[20:21], v[28:29]
	v_pk_mul_f32 v[20:21], v[20:21], s[2:3] op_sel_hi:[1,0]
	v_rcp_f32_e32 v18, v18
	v_exp_f32_e32 v20, v20
	v_exp_f32_e32 v21, v21
	v_rcp_f32_e32 v19, v19
	v_pk_fma_f32 v[26:27], v[122:123], s[52:53], v[10:11] op_sel_hi:[1,0,1]
	v_pk_fma_f32 v[34:35], v[114:115], s[52:53], v[2:3] op_sel_hi:[1,0,1]
	v_pk_add_f32 v[20:21], v[20:21], 1.0 op_sel_hi:[1,0]
	v_pk_mul_f32 v[30:31], v[30:31], v[18:19]
	v_mov_b32_e32 v18, v1
	v_rcp_f32_e32 v20, v20
	v_rcp_f32_e32 v21, v21
	v_cvt_pk_fp8_f32 v18, v30, v31
	v_pk_fma_f32 v[24:25], v[124:125], s[52:53], v[12:13] op_sel_hi:[1,0,1]
	v_pk_fma_f32 v[32:33], v[116:117], s[52:53], v[4:5] op_sel_hi:[1,0,1]
	v_pk_mul_f32 v[20:21], v[28:29], v[20:21]
	v_mov_b32_e32 v19, v1
	v_cvt_pk_fp8_f32 v18, v20, v21 op_sel:[0,0,1]
	v_min_f32_e32 v20, 0x40e00000, v26
	v_min_f32_e32 v21, 0x40e00000, v27
	v_med3_f32 v26, v34, s93, v251
	v_med3_f32 v27, v35, s93, v251
	v_pk_fma_f32 v[26:27], v[26:27], s[0:1], s[0:1] op_sel_hi:[1,0,0]
	v_pk_fma_f32 v[30:31], v[104:105], s[52:53], v[8:9] op_sel_hi:[1,0,1]
	v_pk_mul_f32 v[26:27], v[20:21], v[26:27]
	v_pk_mul_f32 v[20:21], v[20:21], s[2:3] op_sel_hi:[1,0]
	v_med3_f32 v30, v30, s93, v251
	v_exp_f32_e32 v20, v20
	v_exp_f32_e32 v21, v21
	v_med3_f32 v31, v31, s93, v251
	v_pk_fma_f32 v[30:31], v[30:31], s[0:1], s[0:1] op_sel_hi:[1,0,0]
	v_pk_fma_f32 v[28:29], v[106:107], s[52:53], v[10:11] op_sel_hi:[1,0,1]
	v_pk_add_f32 v[20:21], v[20:21], 1.0 op_sel_hi:[1,0]
	v_pk_fma_f32 v[36:37], v[98:99], s[52:53], v[2:3] op_sel_hi:[1,0,1]
	v_rcp_f32_e32 v20, v20
	v_rcp_f32_e32 v21, v21
	v_pk_fma_f32 v[34:35], v[100:101], s[52:53], v[4:5] op_sel_hi:[1,0,1]
	v_add_u32_e32 v23, 0x20000, v23
	v_pk_mul_f32 v[20:21], v[26:27], v[20:21]
	v_pk_fma_f32 v[26:27], v[108:109], s[52:53], v[12:13] op_sel_hi:[1,0,1]
	v_cvt_pk_fp8_f32 v19, v20, v21
	v_min_f32_e32 v20, 0x40e00000, v24
	v_min_f32_e32 v21, 0x40e00000, v25
	v_med3_f32 v24, v32, s93, v251
	v_med3_f32 v25, v33, s93, v251
	v_pk_fma_f32 v[24:25], v[24:25], s[0:1], s[0:1] op_sel_hi:[1,0,0]
	v_pk_fma_f32 v[32:33], v[102:103], s[52:53], v[6:7] op_sel_hi:[1,0,1]
	v_pk_mul_f32 v[24:25], v[20:21], v[24:25]
	v_pk_mul_f32 v[20:21], v[20:21], s[2:3] op_sel_hi:[1,0]
	v_med3_f32 v32, v32, s93, v251
	v_exp_f32_e32 v20, v20
	v_exp_f32_e32 v21, v21
	v_med3_f32 v33, v33, s93, v251
	v_pk_fma_f32 v[32:33], v[32:33], s[0:1], s[0:1] op_sel_hi:[1,0,0]
	v_pk_add_f32 v[20:21], v[20:21], 1.0 op_sel_hi:[1,0]
	s_nop 0
	v_rcp_f32_e32 v20, v20
	v_rcp_f32_e32 v21, v21
	s_nop 0
	v_pk_mul_f32 v[20:21], v[24:25], v[20:21]
	s_nop 0
	v_cvt_pk_fp8_f32 v19, v20, v21 op_sel:[0,0,1]
	v_pk_fma_f32 v[20:21], v[110:111], s[52:53], v[14:15] op_sel_hi:[1,0,1]
	v_pk_fma_f32 v[24:25], v[112:113], s[52:53], v[16:17] op_sel_hi:[1,0,1]
	v_min_f32_e32 v20, 0x40e00000, v20
	v_min_f32_e32 v21, 0x40e00000, v21
	v_pk_mul_f32 v[32:33], v[20:21], v[32:33]
	v_pk_mul_f32 v[20:21], v[20:21], s[2:3] op_sel_hi:[1,0]
	v_min_f32_e32 v24, 0x40e00000, v24
	v_exp_f32_e32 v20, v20
	v_exp_f32_e32 v21, v21
	v_min_f32_e32 v25, 0x40e00000, v25
	v_pk_mul_f32 v[30:31], v[24:25], v[30:31]
	v_pk_mul_f32 v[24:25], v[24:25], s[2:3] op_sel_hi:[1,0]
	v_pk_add_f32 v[20:21], v[20:21], 1.0 op_sel_hi:[1,0]
	v_exp_f32_e32 v24, v24
	v_exp_f32_e32 v25, v25
	v_rcp_f32_e32 v20, v20
	v_rcp_f32_e32 v21, v21
	v_pk_add_f32 v[24:25], v[24:25], 1.0 op_sel_hi:[1,0]
	s_nop 0
	v_rcp_f32_e32 v24, v24
	v_pk_mul_f32 v[32:33], v[32:33], v[20:21]
	v_mov_b32_e32 v20, v1
	v_rcp_f32_e32 v25, v25
	v_cvt_pk_fp8_f32 v20, v32, v33
	v_mov_b32_e32 v21, v1
	v_pk_fma_f32 v[32:33], v[84:85], s[52:53], v[4:5] op_sel_hi:[1,0,1]
	v_pk_mul_f32 v[24:25], v[30:31], v[24:25]
	v_pk_fma_f32 v[30:31], v[86:87], s[52:53], v[6:7] op_sel_hi:[1,0,1]
	v_cvt_pk_fp8_f32 v20, v24, v25 op_sel:[0,0,1]
	v_min_f32_e32 v24, 0x40e00000, v28
	v_min_f32_e32 v25, 0x40e00000, v29
	v_med3_f32 v28, v36, s93, v251
	v_med3_f32 v29, v37, s93, v251
	v_pk_fma_f32 v[28:29], v[28:29], s[0:1], s[0:1] op_sel_hi:[1,0,0]
	v_permlane16_swap_b32_e32 v18, v20
	v_pk_mul_f32 v[28:29], v[24:25], v[28:29]
	v_pk_mul_f32 v[24:25], v[24:25], s[2:3] op_sel_hi:[1,0]
	v_med3_f32 v30, v30, s93, v251
	v_exp_f32_e32 v24, v24
	v_exp_f32_e32 v25, v25
	v_med3_f32 v31, v31, s93, v251
	v_pk_fma_f32 v[30:31], v[30:31], s[0:1], s[0:1] op_sel_hi:[1,0,0]
	v_pk_fma_f32 v[6:7], v[70:71], s[52:53], v[6:7] op_sel_hi:[1,0,1]
	v_pk_add_f32 v[24:25], v[24:25], 1.0 op_sel_hi:[1,0]
	v_med3_f32 v6, v6, s93, v251
	v_rcp_f32_e32 v24, v24
	v_rcp_f32_e32 v25, v25
	v_med3_f32 v7, v7, s93, v251
	v_pk_fma_f32 v[6:7], v[6:7], s[0:1], s[0:1] op_sel_hi:[1,0,0]
;     DI void operator()(const f32x4 (&acc)[2][2][4][2], const Unit& u, int wr, int wc, int fr, int fq) const {
;     ...
;         for (int ai = 0; ai < 2; ++ai) { if (u.half == 2 - ai) continue;
;             u32x2 wprev = {0u, 0u}; const bool oddq = (fq & 1) != 0;
; #pragma unroll
;             for (int m = 0; m < 4; ++m) {
;             f32x4 g0 = acc[ai][0][m][0] * dq + bg0, g1 = acc[ai][0][m][1] * dq + bg1, u0 = acc[ai][1][m][0] * dq + bu0, u1 = acc[ai][1][m][1] * dq + bu1;
;             unsigned wv[2];
; #pragma unroll
;             for (int hv = 0; hv < 2; ++hv) { const f32x4 gq = hv ? g1 : g0, uq = hv ? u1 : u0; int r = 0;
; #pragma unroll
;                 for (int q = 0; q < 4; q += 2) {
;                     f32x2 g = {fminf(gq[q], 7.0f), fminf(gq[q + 1], 7.0f)};
;                     const f32x2 up = {fminf(fmaxf(uq[q], -7.0f), 7.0f), fminf(fmaxf(uq[q + 1], -7.0f), 7.0f)};
;                     f32x2 t = __builtin_elementwise_fma(up, (f32x2){ACT8_SCALE, ACT8_SCALE}, (f32x2){ACT8_SCALE, ACT8_SCALE}) * g;
;                     const f32x2 a = g * (f32x2){-1.702f * 1.4426950408889634f, -1.702f * 1.4426950408889634f};
;                     f32x2 e = {__builtin_amdgcn_exp2f(a[0]), __builtin_amdgcn_exp2f(a[1])}; e = e + (f32x2){1.0f, 1.0f};
;                     const f32x2 rc = {__builtin_amdgcn_rcpf(e[0]), __builtin_amdgcn_rcpf(e[1])};
;                     t = t * rc;
;                     r = q ? __builtin_amdgcn_cvt_pk_fp8_f32(t[0], t[1], r, true) : __builtin_amdgcn_cvt_pk_fp8_f32(t[0], t[1], r, false); }
;                 wv[hv] = (unsigned)r; }
;             u32x2 w; w.x = wv[0]; w.y = wv[1];
;             if ((m & 1) == 0) wprev = w;
;             else {
;                 const auto rx = __builtin_amdgcn_permlane16_swap(wprev.x, w.x, false, false), ry = __builtin_amdgcn_permlane16_swap(wprev.y, w.y, false, false);
;                 u32x4 ww; ww.x = rx[0]; ww.y = ry[0]; ww.z = rx[1]; ww.w = ry[1];
;                 const unsigned off = (unsigned)((128 * ai + 16 * (m - 1 + (oddq ? 1 : 0)) + lrow) * DFF + cj - (oddq ? 8 : 0));
;                 *(u32x4*)(abase + off) = ww; }
;             asm volatile("" ::: "memory"); } }
	v_pk_fma_f32 v[4:5], v[68:69], s[52:53], v[4:5] op_sel_hi:[1,0,1]
	v_pk_mul_f32 v[24:25], v[28:29], v[24:25]
	v_pk_fma_f32 v[28:29], v[88:89], s[52:53], v[8:9] op_sel_hi:[1,0,1]
	v_cvt_pk_fp8_f32 v21, v24, v25
	v_min_f32_e32 v24, 0x40e00000, v26
	v_min_f32_e32 v25, 0x40e00000, v27
	v_med3_f32 v26, v34, s93, v251
	v_med3_f32 v27, v35, s93, v251
	v_pk_fma_f32 v[26:27], v[26:27], s[0:1], s[0:1] op_sel_hi:[1,0,0]
	v_med3_f32 v28, v28, s93, v251
	v_pk_mul_f32 v[26:27], v[24:25], v[26:27]
	v_pk_mul_f32 v[24:25], v[24:25], s[2:3] op_sel_hi:[1,0]
	v_med3_f32 v29, v29, s93, v251
	v_exp_f32_e32 v24, v24
	v_exp_f32_e32 v25, v25
	v_pk_fma_f32 v[28:29], v[28:29], s[0:1], s[0:1] op_sel_hi:[1,0,0]
	v_pk_fma_f32 v[34:35], v[82:83], s[52:53], v[2:3] op_sel_hi:[1,0,1]
	v_pk_fma_f32 v[8:9], v[72:73], s[52:53], v[8:9] op_sel_hi:[1,0,1]
	v_pk_add_f32 v[24:25], v[24:25], 1.0 op_sel_hi:[1,0]
	v_med3_f32 v8, v8, s93, v251
	v_rcp_f32_e32 v24, v24
	v_rcp_f32_e32 v25, v25
	v_med3_f32 v9, v9, s93, v251
	v_pk_fma_f32 v[8:9], v[8:9], s[0:1], s[0:1] op_sel_hi:[1,0,0]
	v_pk_fma_f32 v[2:3], v[66:67], s[52:53], v[2:3] op_sel_hi:[1,0,1]
	v_pk_mul_f32 v[24:25], v[26:27], v[24:25]
	v_pk_fma_f32 v[26:27], v[90:91], s[52:53], v[10:11] op_sel_hi:[1,0,1]
	v_cvt_pk_fp8_f32 v21, v24, v25 op_sel:[0,0,1]
	v_add3_u32 v24, v23, v0, v22
	v_pk_fma_f32 v[10:11], v[74:75], s[52:53], v[10:11] op_sel_hi:[1,0,1]
	v_med3_f32 v2, v2, s93, v251
	v_permlane16_swap_b32_e32 v19, v21
	global_store_dwordx4 v24, v[18:21], s[6:7] nt
	v_pk_fma_f32 v[24:25], v[92:93], s[52:53], v[12:13] op_sel_hi:[1,0,1]
	v_med3_f32 v3, v3, s93, v251
	v_pk_fma_f32 v[18:19], v[94:95], s[52:53], v[14:15] op_sel_hi:[1,0,1]
	v_pk_fma_f32 v[20:21], v[96:97], s[52:53], v[16:17] op_sel_hi:[1,0,1]
	v_min_f32_e32 v18, 0x40e00000, v18
	v_min_f32_e32 v19, 0x40e00000, v19
	v_pk_mul_f32 v[30:31], v[18:19], v[30:31]
	v_pk_mul_f32 v[18:19], v[18:19], s[2:3] op_sel_hi:[1,0]
	v_min_f32_e32 v20, 0x40e00000, v20
	v_exp_f32_e32 v18, v18
	v_exp_f32_e32 v19, v19
	v_min_f32_e32 v21, 0x40e00000, v21
	v_pk_mul_f32 v[28:29], v[20:21], v[28:29]
	v_pk_mul_f32 v[20:21], v[20:21], s[2:3] op_sel_hi:[1,0]
	v_pk_add_f32 v[18:19], v[18:19], 1.0 op_sel_hi:[1,0]
	v_exp_f32_e32 v20, v20
	v_exp_f32_e32 v21, v21
	v_rcp_f32_e32 v18, v18
	v_rcp_f32_e32 v19, v19
	v_pk_fma_f32 v[14:15], v[78:79], s[52:53], v[14:15] op_sel_hi:[1,0,1]
	v_pk_add_f32 v[20:21], v[20:21], 1.0 op_sel_hi:[1,0]
	v_min_f32_e32 v14, 0x40e00000, v14
	v_pk_mul_f32 v[30:31], v[30:31], v[18:19]
	v_mov_b32_e32 v18, v1
	v_rcp_f32_e32 v20, v20
	v_rcp_f32_e32 v21, v21
	v_cvt_pk_fp8_f32 v18, v30, v31
	v_mov_b32_e32 v19, v1
	v_min_f32_e32 v15, 0x40e00000, v15
	v_pk_mul_f32 v[20:21], v[28:29], v[20:21]
	v_pk_mul_f32 v[6:7], v[14:15], v[6:7]
	v_cvt_pk_fp8_f32 v18, v20, v21 op_sel:[0,0,1]
	v_min_f32_e32 v20, 0x40e00000, v26
	v_min_f32_e32 v21, 0x40e00000, v27
	v_med3_f32 v26, v34, s93, v251
	v_med3_f32 v27, v35, s93, v251
	v_pk_fma_f32 v[26:27], v[26:27], s[0:1], s[0:1] op_sel_hi:[1,0,0]
	v_pk_mul_f32 v[14:15], v[14:15], s[2:3] op_sel_hi:[1,0]
	v_pk_mul_f32 v[26:27], v[20:21], v[26:27]
	v_pk_mul_f32 v[20:21], v[20:21], s[2:3] op_sel_hi:[1,0]
	v_exp_f32_e32 v14, v14
	v_exp_f32_e32 v20, v20
	v_exp_f32_e32 v21, v21
	v_exp_f32_e32 v15, v15
	v_pk_fma_f32 v[16:17], v[80:81], s[52:53], v[16:17] op_sel_hi:[1,0,1]
	v_pk_fma_f32 v[2:3], v[2:3], s[0:1], s[0:1] op_sel_hi:[1,0,0]
	v_pk_add_f32 v[20:21], v[20:21], 1.0 op_sel_hi:[1,0]
	v_pk_add_f32 v[14:15], v[14:15], 1.0 op_sel_hi:[1,0]
	v_rcp_f32_e32 v20, v20
	v_rcp_f32_e32 v21, v21
	v_rcp_f32_e32 v14, v14
	v_rcp_f32_e32 v15, v15
	v_pk_fma_f32 v[12:13], v[76:77], s[52:53], v[12:13] op_sel_hi:[1,0,1]
	v_pk_mul_f32 v[20:21], v[26:27], v[20:21]
	v_med3_f32 v4, v4, s93, v251
	v_cvt_pk_fp8_f32 v19, v20, v21
	v_min_f32_e32 v20, 0x40e00000, v24
	v_min_f32_e32 v21, 0x40e00000, v25
	v_med3_f32 v24, v32, s93, v251
	v_med3_f32 v25, v33, s93, v251
	v_pk_fma_f32 v[24:25], v[24:25], s[0:1], s[0:1] op_sel_hi:[1,0,0]
	v_pk_mul_f32 v[6:7], v[6:7], v[14:15]
	v_pk_mul_f32 v[24:25], v[20:21], v[24:25]
	v_pk_mul_f32 v[20:21], v[20:21], s[2:3] op_sel_hi:[1,0]
	v_med3_f32 v5, v5, s93, v251
	v_exp_f32_e32 v20, v20
	v_exp_f32_e32 v21, v21
	v_pk_fma_f32 v[4:5], v[4:5], s[0:1], s[0:1] op_sel_hi:[1,0,0]
	v_add_u32_e32 v0, v0, v22
	s_mov_b32 s0, 0x8000
	v_pk_add_f32 v[20:21], v[20:21], 1.0 op_sel_hi:[1,0]
	v_add3_u32 v0, v0, v23, s0
	v_rcp_f32_e32 v20, v20
	v_rcp_f32_e32 v21, v21
	s_nop 0
	v_pk_mul_f32 v[20:21], v[24:25], v[20:21]
	s_nop 0
	v_cvt_pk_fp8_f32 v19, v20, v21 op_sel:[0,0,1]
	v_mov_b32_e32 v20, v1
	v_cvt_pk_fp8_f32 v20, v6, v7
	v_min_f32_e32 v6, 0x40e00000, v16
	v_min_f32_e32 v7, 0x40e00000, v17
	v_pk_mul_f32 v[8:9], v[6:7], v[8:9]
	v_pk_mul_f32 v[6:7], v[6:7], s[2:3] op_sel_hi:[1,0]
	v_mov_b32_e32 v21, v1
	v_exp_f32_e32 v6, v6
	v_exp_f32_e32 v7, v7
	s_nop 0
	v_pk_add_f32 v[6:7], v[6:7], 1.0 op_sel_hi:[1,0]
	s_nop 0
	v_rcp_f32_e32 v6, v6
	v_rcp_f32_e32 v7, v7
	s_nop 0
	v_pk_mul_f32 v[6:7], v[8:9], v[6:7]
	s_nop 0
	v_cvt_pk_fp8_f32 v20, v6, v7 op_sel:[0,0,1]
	v_min_f32_e32 v6, 0x40e00000, v10
	v_min_f32_e32 v7, 0x40e00000, v11
	v_pk_mul_f32 v[2:3], v[6:7], v[2:3]
	v_pk_mul_f32 v[6:7], v[6:7], s[2:3] op_sel_hi:[1,0]
	v_permlane16_swap_b32_e32 v18, v20
	v_exp_f32_e32 v6, v6
	v_exp_f32_e32 v7, v7
	s_nop 0
	v_pk_add_f32 v[6:7], v[6:7], 1.0 op_sel_hi:[1,0]
	s_nop 0
	v_rcp_f32_e32 v6, v6
	v_rcp_f32_e32 v7, v7
	s_nop 0
	v_pk_mul_f32 v[2:3], v[2:3], v[6:7]
	s_nop 0
	v_cvt_pk_fp8_f32 v21, v2, v3
	v_min_f32_e32 v2, 0x40e00000, v12
	v_min_f32_e32 v3, 0x40e00000, v13
	v_pk_mul_f32 v[4:5], v[2:3], v[4:5]
	v_pk_mul_f32 v[2:3], v[2:3], s[2:3] op_sel_hi:[1,0]
	s_nop 0
	v_exp_f32_e32 v2, v2
	v_exp_f32_e32 v3, v3
	s_nop 0
	v_pk_add_f32 v[2:3], v[2:3], 1.0 op_sel_hi:[1,0]
	s_nop 0
	v_rcp_f32_e32 v2, v2
	v_rcp_f32_e32 v3, v3
	s_nop 0
	v_pk_mul_f32 v[2:3], v[4:5], v[2:3]
	s_nop 0
	v_cvt_pk_fp8_f32 v21, v2, v3 op_sel:[0,0,1]
	s_nop 1
	v_permlane16_swap_b32_e32 v19, v21
	global_store_dwordx4 v0, v[18:21], s[6:7] nt
	s_and_b64 vcc, exec, s[4:5]
	s_mov_b64 s[2:3], -1
	s_cbranch_vccnz .LBB0_1201
	s_branch .LBB0_1239
